# speedup vs baseline: 1.0041x; 1.0041x over previous
.LBB2_5:
	ds_read_b128 v[102:105], v120 offset:8192
	ds_read_b128 v[106:109], v120 offset:10240
	ds_read_b128 v[110:113], v120 offset:12288
	v_exp_f32_e32 v69, v46
	v_exp_f32_e32 v71, v47
	v_exp_f32_e32 v73, v48
	v_exp_f32_e32 v75, v49
	ds_read_b128 v[46:49], v120 offset:14336
	v_exp_f32_e32 v42, v42
	v_exp_f32_e32 v43, v43
	v_exp_f32_e32 v44, v44
	v_exp_f32_e32 v45, v45
	v_cvt_pk_f16_f32 v76, v69, v71
	v_cvt_pk_f16_f32 v77, v73, v75
	v_cvt_pk_f16_f32 v78, v42, v43
	v_cvt_pk_f16_f32 v79, v44, v45
	ds_read_b128 v[42:45], v121 offset:8192
	v_exp_f32_e32 v38, v38
	v_exp_f32_e32 v39, v39
	s_waitcnt lgkmcnt(4)
	v_mfma_f32_16x16x32_f16 v[26:29], v[102:105], v[76:79], v[26:29]
	v_exp_f32_e32 v40, v40
	v_exp_f32_e32 v41, v41
	s_waitcnt lgkmcnt(3)
	v_mfma_f32_16x16x32_f16 v[22:25], v[106:109], v[76:79], v[22:25]
	ds_read_b128 v[102:105], v121 offset:10240
	v_exp_f32_e32 v34, v34
	v_exp_f32_e32 v35, v35
	s_waitcnt lgkmcnt(3)
	v_mfma_f32_16x16x32_f16 v[18:21], v[110:113], v[76:79], v[18:21]
	ds_read_b128 v[106:109], v121 offset:12288
	v_exp_f32_e32 v36, v36
	v_exp_f32_e32 v37, v37
	s_waitcnt lgkmcnt(3)
	v_mfma_f32_16x16x32_f16 v[10:13], v[46:49], v[76:79], v[10:13]
	ds_read_b128 v[110:113], v121 offset:14336
	v_mfma_f32_16x16x32_f16 v[14:17], v[116:119], v[76:79], v[14:17]
	v_cvt_pk_f16_f32 v37, v36, v37
	v_cvt_pk_f16_f32 v36, v34, v35
	v_cvt_pk_f16_f32 v35, v40, v41
	v_cvt_pk_f16_f32 v34, v38, v39
	s_mov_b64 s[38:39], 0
	s_waitcnt lgkmcnt(3)
	v_mfma_f32_16x16x32_f16 v[26:29], v[42:45], v[34:37], v[26:29]
	s_waitcnt lgkmcnt(2)
	v_mfma_f32_16x16x32_f16 v[22:25], v[102:105], v[34:37], v[22:25]
	s_waitcnt lgkmcnt(1)
	v_mfma_f32_16x16x32_f16 v[18:21], v[106:109], v[34:37], v[18:21]
	s_waitcnt lgkmcnt(0)
	v_mfma_f32_16x16x32_f16 v[10:13], v[110:113], v[34:37], v[10:13]
	v_mfma_f32_16x16x32_f16 v[14:17], v[116:119], v[34:37], v[14:17]
	s_cmp_eq_u32 s55, 0
	s_cbranch_scc1 .LBB2_6
	s_mov_b32 s80, 0
	s_cmp_eq_u32 s81, 0
	s_cbranch_scc1 .Lattn_A
	s_branch .Lattn_post
	.p2align 3
